# v9 + nt on prologue weight loads/stores + Y8 stores nt only for tile rounds 0-1 (later rounds stay in MALL for the combine)
# speedup vs baseline: 1.0163x; 1.0163x over previous
; #define LAS __attribute__((address_space(3)))
; DI unsigned pk_bf16(float lo, float hi) { const f32x2 v = {lo, hi}; return __builtin_bit_cast(unsigned, __builtin_convertvector(v, bf16x2_t)); }
; DI void tr_tile(const float* src, int N, int k0, int n0, float scale, bf16_t* dst_row0  , int K, bf16_t* dst_lo, LAS bf16_t* T, int lane) {
; #pragma unroll 4
;     for (int it = 0; it < 8; ++it) {
;         const int kk = it * 8 + 2 * (lane >> 4), c4 = (lane & 15) * 4;
;         const f32x4 v0 = *(const f32x4*)(src + (size_t)(k0 + kk) * N + n0 + c4) * scale, v1 = *(const f32x4*)(src + (size_t)(k0 + kk + 1) * N + n0 + c4) * scale;
; #pragma unroll
;         for (int j = 0; j < 4; ++j) *(LAS unsigned*)(T + (c4 + j) * 72 + kk) = pk_bf16(v0[j], v1[j]);
;     }
;     __builtin_amdgcn_s_waitcnt(0xc07f);
; #pragma unroll 4
;     for (int it = 0; it < 8; ++it) {
;         const int n = it * 8 + (lane >> 3), kc = (lane & 7) * 8;
;         const u32x4 w = *(const LAS u32x4*)(T + n * 72 + kc);
;         *(u32x4*)(dst_row0 + (size_t)n * K + kc) = w;
.LBB0_43:
	v_add_u32_e32 v23, s71, v41
	v_ashrrev_i32_e32 v27, 31, v23
	v_mad_u64_u32 v[24:25], s[82:83], v23, s72, 0
	v_add_u32_e32 v28, 1, v23
	v_add_u32_e32 v30, 8, v23
	v_add_u32_e32 v32, 9, v23
	v_add_u32_e32 v34, 16, v23
	v_add_u32_e32 v36, 17, v23
	v_add_u32_e32 v42, 24, v23
	v_add_u32_e32 v23, 25, v23
	v_mov_b32_e32 v26, v25
	v_ashrrev_i32_e32 v47, 31, v28
	v_mad_u64_u32 v[28:29], s[82:83], v28, s72, 0
	v_ashrrev_i32_e32 v49, 31, v30
	v_mad_u64_u32 v[30:31], s[82:83], v30, s72, 0
	v_ashrrev_i32_e32 v51, 31, v32
	v_mad_u64_u32 v[32:33], s[82:83], v32, s72, 0
	v_ashrrev_i32_e32 v53, 31, v34
	v_mad_u64_u32 v[34:35], s[82:83], v34, s72, 0
	v_ashrrev_i32_e32 v55, 31, v36
	v_mad_u64_u32 v[36:37], s[82:83], v36, s72, 0
	v_ashrrev_i32_e32 v57, 31, v42
	v_mad_u64_u32 v[42:43], s[82:83], v42, s72, 0
	v_mad_u64_u32 v[44:45], s[82:83], v23, s72, 0
	v_ashrrev_i32_e32 v59, 31, v23
	v_mad_u64_u32 v[26:27], s[82:83], v27, s72, v[26:27]
	v_mov_b32_e32 v46, v29
	v_mov_b32_e32 v48, v31
	v_mov_b32_e32 v50, v33
	v_mov_b32_e32 v52, v35
	v_mov_b32_e32 v54, v37
	v_mov_b32_e32 v56, v43
	v_mov_b32_e32 v58, v45
	v_mov_b32_e32 v25, v26
	v_mad_u64_u32 v[26:27], s[82:83], v47, s72, v[46:47]
	v_mad_u64_u32 v[46:47], s[82:83], v49, s72, v[48:49]
	v_mad_u64_u32 v[48:49], s[82:83], v51, s72, v[50:51]
	v_mad_u64_u32 v[50:51], s[82:83], v53, s72, v[52:53]
	v_mad_u64_u32 v[52:53], s[82:83], v55, s72, v[54:55]
	v_mad_u64_u32 v[54:55], s[82:83], v57, s72, v[56:57]
	v_mad_u64_u32 v[56:57], s[82:83], v59, s72, v[58:59]
	v_lshl_add_u64 v[24:25], v[24:25], 2, v[20:21]
	v_mov_b32_e32 v29, v26
	v_mov_b32_e32 v31, v46
	v_mov_b32_e32 v33, v48
	v_mov_b32_e32 v35, v50
	v_mov_b32_e32 v43, v54
	v_mov_b32_e32 v45, v56
	v_mov_b32_e32 v37, v52
	global_load_dwordx4 v[24:27], v[24:25], off nt
	v_lshl_add_u64 v[28:29], v[28:29], 2, v[20:21]
	v_lshl_add_u64 v[46:47], v[30:31], 2, v[20:21]
	v_lshl_add_u64 v[48:49], v[32:33], 2, v[20:21]
	v_lshl_add_u64 v[50:51], v[34:35], 2, v[20:21]
	v_lshl_add_u64 v[54:55], v[42:43], 2, v[20:21]
	v_lshl_add_u64 v[58:59], v[44:45], 2, v[20:21]
	v_lshl_add_u64 v[36:37], v[36:37], 2, v[20:21]
	global_load_dwordx4 v[28:31], v[28:29], off nt
	s_nop 0
	global_load_dwordx4 v[32:35], v[46:47], off nt
	global_load_dwordx4 v[42:45], v[48:49], off nt
	s_nop 0
	global_load_dwordx4 v[46:49], v[50:51], off nt
	s_nop 0
	global_load_dwordx4 v[50:53], v[36:37], off nt
	s_nop 0
	global_load_dwordx4 v[54:57], v[54:55], off nt
	s_nop 0
	global_load_dwordx4 v[58:61], v[58:59], off nt
	s_add_i32 s71, s71, 32
	s_cmp_eq_u32 s71, 64
	s_waitcnt vmcnt(0)
	v_mov_b32_e32 v36, v24
	v_mov_b32_e32 v24, v26
	v_mov_b32_e32 v37, v28
	v_mov_b32_e32 v28, v25
	v_mov_b32_e32 v25, v30
	v_mov_b32_e32 v30, v27
	v_mov_b32_e32 v26, v32
	v_mov_b32_e32 v27, v42
	v_mov_b32_e32 v42, v33
	v_mov_b32_e32 v32, v34
	v_mov_b32_e32 v33, v44
	v_mov_b32_e32 v44, v35
	v_mov_b32_e32 v34, v46
	v_mov_b32_e32 v35, v50
	v_mov_b32_e32 v50, v47
	v_mov_b32_e32 v46, v48
	v_mov_b32_e32 v47, v52
	v_mov_b32_e32 v52, v49
	v_mov_b32_e32 v48, v54
	v_mov_b32_e32 v49, v58
	v_mov_b32_e32 v58, v55
	v_mov_b32_e32 v54, v56
	v_mov_b32_e32 v55, v60
	v_mov_b32_e32 v60, v57
	v_pk_mul_f32 v[36:37], v[18:19], v[36:37]
	v_pk_mul_f32 v[26:27], v[18:19], v[26:27]
	v_pk_mul_f32 v[28:29], v[18:19], v[28:29]
	v_pk_mul_f32 v[24:25], v[18:19], v[24:25]
	v_pk_mul_f32 v[30:31], v[18:19], v[30:31]
	v_pk_mul_f32 v[42:43], v[18:19], v[42:43]
	v_pk_mul_f32 v[32:33], v[18:19], v[32:33]
	v_pk_mul_f32 v[44:45], v[18:19], v[44:45]
	v_pk_mul_f32 v[34:35], v[18:19], v[34:35]
	v_pk_mul_f32 v[50:51], v[18:19], v[50:51]
	v_pk_mul_f32 v[46:47], v[18:19], v[46:47]
	v_pk_mul_f32 v[52:53], v[18:19], v[52:53]
	v_pk_mul_f32 v[48:49], v[18:19], v[48:49]
	v_pk_mul_f32 v[56:57], v[18:19], v[58:59]
	v_pk_mul_f32 v[54:55], v[18:19], v[54:55]
	v_pk_mul_f32 v[58:59], v[18:19], v[60:61]
	v_cvt_pk_bf16_f32 v23, v36, v37
	v_cvt_pk_bf16_f32 v26, v26, v27
	v_cvt_pk_bf16_f32 v28, v28, v29
	v_cvt_pk_bf16_f32 v24, v24, v25
	v_cvt_pk_bf16_f32 v25, v30, v31
	v_cvt_pk_bf16_f32 v27, v42, v43
	v_cvt_pk_bf16_f32 v29, v32, v33
	v_cvt_pk_bf16_f32 v30, v44, v45
	v_cvt_pk_bf16_f32 v31, v34, v35
	v_cvt_pk_bf16_f32 v32, v50, v51
	v_cvt_pk_bf16_f32 v33, v46, v47
	v_cvt_pk_bf16_f32 v34, v52, v53
	v_cvt_pk_bf16_f32 v35, v48, v49
	v_cvt_pk_bf16_f32 v36, v56, v57
	v_cvt_pk_bf16_f32 v37, v54, v55
	v_cvt_pk_bf16_f32 v42, v58, v59
	ds_write2_b32 v22, v23, v26 offset1:4
	ds_write2_b32 v22, v28, v27 offset0:36 offset1:40
	ds_write2_b32 v22, v24, v29 offset0:72 offset1:76
	ds_write2_b32 v22, v25, v30 offset0:108 offset1:112
	ds_write2_b32 v22, v31, v35 offset0:8 offset1:12
	ds_write2_b32 v22, v32, v36 offset0:44 offset1:48
	ds_write2_b32 v22, v33, v37 offset0:80 offset1:84
	ds_write2_b32 v22, v34, v42 offset0:116 offset1:120
	v_add_u32_e32 v22, 64, v22
	s_cbranch_scc0 .LBB0_43
	s_lshl_b32 s71, s81, 7
	s_lshl_b32 s81, s81, 5
	s_and_b32 s71, s71, 0x100
	s_and_b32 s81, s81, 0xffffff80
	s_add_i32 s71, s71, s81
	s_and_b32 s81, s70, 64
	s_or_b32 s71, s71, s81
	s_lshl_b32 s80, s80, 6
	s_and_b64 s[82:83], s[60:61], exec
	s_cselect_b32 s82, s71, s70
	s_ashr_i32 s83, s82, 31
	s_ashr_i32 s81, s80, 31
	s_lshl_b64 s[70:71], s[80:81], 1
	s_lshl_b64 s[80:81], s[82:83], 1
	v_lshl_add_u64 v[22:23], v[6:7], 0, s[80:81]
	v_mad_u64_u32 v[24:25], s[82:83], s22, v22, 0
	v_mov_b32_e32 v22, v25
	v_mad_u64_u32 v[22:23], s[82:83], s22, v23, v[22:23]
	v_mov_b32_e32 v25, v22
	v_mov_b32_e32 v42, s78
	v_mad_u64_u32 v[22:23], s[82:83], s66, v42, v[24:25]
	s_mul_i32 s78, s67, s78
	s_mul_i32 s79, s66, s79
	v_lshl_add_u64 v[24:25], v[8:9], 0, s[80:81]
	s_add_i32 s82, s79, s78
	v_mad_u64_u32 v[26:27], s[78:79], s22, v24, 0
	v_mov_b32_e32 v24, v27
	v_mad_u64_u32 v[24:25], s[78:79], s22, v25, v[24:25]
	v_mov_b32_e32 v27, v24
	v_mad_u64_u32 v[24:25], s[78:79], s66, v42, v[26:27]
	v_lshl_add_u64 v[26:27], v[10:11], 0, s[80:81]
	v_mad_u64_u32 v[28:29], s[78:79], s22, v26, 0
	v_mov_b32_e32 v26, v29
	v_mad_u64_u32 v[26:27], s[78:79], s22, v27, v[26:27]
	v_mov_b32_e32 v29, v26
	v_mad_u64_u32 v[26:27], s[78:79], s66, v42, v[28:29]
	v_lshl_add_u64 v[28:29], v[2:3], 0, s[80:81]
	v_mad_u64_u32 v[36:37], s[78:79], s22, v28, 0
	v_mov_b32_e32 v28, v37
	v_mad_u64_u32 v[28:29], s[78:79], s22, v29, v[28:29]
	v_mov_b32_e32 v37, v28
	v_mad_u64_u32 v[28:29], s[78:79], s66, v42, v[36:37]
	v_add_u32_e32 v23, s82, v23
	v_add_u32_e32 v25, s82, v25
	v_add_u32_e32 v27, s82, v27
	v_add_u32_e32 v29, s82, v29
	v_lshl_add_u64 v[30:31], v[16:17], 0, v[22:23]
	v_lshl_add_u64 v[32:33], v[16:17], 0, v[24:25]
	v_lshl_add_u64 v[34:35], v[16:17], 0, v[26:27]
	v_lshl_add_u64 v[36:37], v[16:17], 0, v[28:29]
	s_mov_b32 s78, 0
	s_waitcnt lgkmcnt(0)
; #define LAS __attribute__((address_space(3)))
; DI void tr_tile(const float* src, int N, int k0, int n0, float scale, bf16_t* dst_row0  , int K, bf16_t* dst_lo, LAS bf16_t* T, int lane) {
;     ...
; #pragma unroll 4
;     for (int it = 0; it < 8; ++it) {
;         const int n = it * 8 + (lane >> 3), kc = (lane & 7) * 8;
;         const u32x4 w = *(const LAS u32x4*)(T + n * 72 + kc);
;         *(u32x4*)(dst_row0 + (size_t)n * K + kc) = w;
;     }
.LBB0_45:
	s_nop 0
	v_add_u32_e32 v54, s78, v39
	ds_read_b128 v[42:45], v54
	ds_read_b128 v[46:49], v54 offset:1152
	ds_read_b128 v[50:53], v54 offset:2304
	ds_read_b128 v[54:57], v54 offset:3456
	s_addk_i32 s78, 0x1200
	v_lshl_add_u64 v[58:59], v[36:37], 0, s[70:71]
	v_lshl_add_u64 v[60:61], v[34:35], 0, s[70:71]
	v_lshl_add_u64 v[62:63], v[32:33], 0, s[70:71]
	v_lshl_add_u64 v[64:65], v[30:31], 0, s[70:71]
	v_lshl_add_u64 v[30:31], v[30:31], 0, s[68:69]
	v_lshl_add_u64 v[32:33], v[32:33], 0, s[68:69]
	v_lshl_add_u64 v[34:35], v[34:35], 0, s[68:69]
	v_lshl_add_u64 v[36:37], v[36:37], 0, s[68:69]
	s_cmpk_eq_i32 s78, 0x2400
	s_waitcnt lgkmcnt(3)
	global_store_dwordx4 v[58:59], v[42:45], off nt
	s_waitcnt lgkmcnt(2)
	global_store_dwordx4 v[60:61], v[46:49], off nt
	s_waitcnt lgkmcnt(1)
	global_store_dwordx4 v[62:63], v[50:53], off nt
	s_waitcnt lgkmcnt(0)
	global_store_dwordx4 v[64:65], v[54:57], off nt
	s_cbranch_scc0 .LBB0_45
	s_and_b64 vcc, exec, s[56:57]
	s_cbranch_vccz .LBB0_41
	s_mov_b32 s78, 0
	v_mov_b32_e32 v30, v38
	s_waitcnt lgkmcnt(0)

.LBB0_1282:
	s_add_i32 s18, s30, 0x2000
	s_mov_b32 m0, s30
	v_lshl_add_u64 v[72:73], s[16:17], 0, v[176:177]
	s_add_u32 s6, s16, 0x4000
	global_load_lds_dwordx4 v[72:73], off
	v_lshl_add_u64 v[72:73], s[16:17], 0, v[64:65]
	s_mov_b32 m0, s18
	s_addc_u32 s7, s17, 0
	s_add_i32 s19, s30, 0x4000
	global_load_lds_dwordx4 v[72:73], off
	v_lshl_add_u64 v[72:73], s[6:7], 0, v[176:177]
	s_mov_b32 m0, s19
	s_add_i32 s31, s30, 0x6000
	global_load_lds_dwordx4 v[72:73], off
	v_lshl_add_u64 v[72:73], s[6:7], 0, v[64:65]
	s_add_u32 s6, s16, 0x8000
	s_mov_b32 m0, s31
	s_addc_u32 s7, s17, 0
	s_add_i32 s36, s30, 0x8000
	global_load_lds_dwordx4 v[72:73], off
	v_lshl_add_u64 v[72:73], s[6:7], 0, v[176:177]
	s_mov_b32 m0, s36
	s_add_i32 s37, s30, 0xa000
	s_waitcnt vmcnt(0)
	s_waitcnt vmcnt(0)
	s_barrier
	global_load_lds_dwordx4 v[72:73], off
	v_lshl_add_u64 v[72:73], s[6:7], 0, v[64:65]
	s_add_u32 s6, s16, 0xc000
	s_mov_b32 m0, s37
	s_addc_u32 s7, s17, 0
	s_add_i32 s38, s30, 0xc000
	global_load_lds_dwordx4 v[72:73], off
	v_lshl_add_u64 v[72:73], s[6:7], 0, v[176:177]
	s_mov_b32 m0, s38
	s_add_i32 s39, s30, 0xe000
	global_load_lds_dwordx4 v[72:73], off
	v_lshl_add_u64 v[72:73], s[6:7], 0, v[64:65]
	s_mov_b32 m0, s39
	s_nop 0
	global_load_lds_dwordx4 v[72:73], off
	ds_read_b128 v[72:75], v94
	ds_read_b128 v[76:79], v94 offset:8192
	ds_read_b128 v[80:83], v95
	ds_read_b128 v[106:109], v95 offset:8192
	ds_read_b128 v[110:113], v96
	ds_read_b128 v[114:117], v96 offset:8192
	ds_read_b128 v[118:121], v97
	ds_read_b128 v[122:125], v97 offset:8192
	ds_read_b128 v[126:129], v98
	ds_read_b128 v[130:133], v98 offset:8192
	ds_read_b128 v[134:137], v99
	ds_read_b128 v[138:141], v99 offset:8192
	ds_read_b128 v[142:145], v100
	ds_read_b128 v[146:149], v100 offset:8192
	ds_read_b128 v[150:153], v101
	ds_read_b128 v[154:157], v101 offset:8192
	s_setprio 1
	s_waitcnt lgkmcnt(0)
	v_mfma_f32_16x16x32_bf16 v[158:161], v[72:75], v[0:3], 0
	v_mfma_f32_16x16x32_bf16 v[162:165], v[76:79], v[0:3], 0
	v_mfma_f32_16x16x32_bf16 v[72:75], v[72:75], v[32:35], 0
	v_mfma_f32_16x16x32_bf16 v[76:79], v[76:79], v[32:35], 0
	v_mfma_f32_16x16x32_bf16 v[162:165], v[106:109], v[4:7], v[162:165]
	v_mfma_f32_16x16x32_bf16 v[72:75], v[80:83], v[36:39], v[72:75]
	v_mfma_f32_16x16x32_bf16 v[76:79], v[106:109], v[36:39], v[76:79]
	v_mfma_f32_16x16x32_bf16 v[158:161], v[80:83], v[4:7], v[158:161]
	v_mfma_f32_16x16x32_bf16 v[106:109], v[114:117], v[8:11], v[162:165]
	v_mfma_f32_16x16x32_bf16 v[72:75], v[110:113], v[40:43], v[72:75]
	v_mfma_f32_16x16x32_bf16 v[76:79], v[114:117], v[40:43], v[76:79]
	v_mfma_f32_16x16x32_bf16 v[80:83], v[110:113], v[8:11], v[158:161]
	v_mfma_f32_16x16x32_bf16 v[106:109], v[122:125], v[12:15], v[106:109]
	v_mfma_f32_16x16x32_bf16 v[72:75], v[118:121], v[44:47], v[72:75]
	v_mfma_f32_16x16x32_bf16 v[76:79], v[122:125], v[44:47], v[76:79]
	v_mfma_f32_16x16x32_bf16 v[80:83], v[118:121], v[12:15], v[80:83]
	v_mfma_f32_16x16x32_bf16 v[106:109], v[130:133], v[16:19], v[106:109]
	v_mfma_f32_16x16x32_bf16 v[72:75], v[126:129], v[48:51], v[72:75]
	v_mfma_f32_16x16x32_bf16 v[76:79], v[130:133], v[48:51], v[76:79]
	v_mfma_f32_16x16x32_bf16 v[80:83], v[126:129], v[16:19], v[80:83]
	v_mfma_f32_16x16x32_bf16 v[106:109], v[138:141], v[20:23], v[106:109]
	v_mfma_f32_16x16x32_bf16 v[72:75], v[134:137], v[52:55], v[72:75]
	v_mfma_f32_16x16x32_bf16 v[76:79], v[138:141], v[52:55], v[76:79]
	v_mfma_f32_16x16x32_bf16 v[80:83], v[134:137], v[20:23], v[80:83]
	v_mfma_f32_16x16x32_bf16 v[106:109], v[146:149], v[24:27], v[106:109]
	v_mfma_f32_16x16x32_bf16 v[72:75], v[142:145], v[56:59], v[72:75]
	v_mfma_f32_16x16x32_bf16 v[76:79], v[146:149], v[56:59], v[76:79]
	v_mfma_f32_16x16x32_bf16 v[80:83], v[142:145], v[24:27], v[80:83]
	v_mfma_f32_16x16x32_bf16 v[106:109], v[154:157], v[28:31], v[106:109]
	v_mfma_f32_16x16x32_bf16 v[72:75], v[150:153], v[60:63], v[72:75]
	v_mfma_f32_16x16x32_bf16 v[76:79], v[154:157], v[60:63], v[76:79]
	v_mfma_f32_16x16x32_bf16 v[80:83], v[150:153], v[28:31], v[80:83]
	s_setprio 0
	s_nop 6
	v_max_f32_e64 v84, |v81|, |v81|
	v_max_f32_e64 v85, |v80|, |v80|
	v_max_f32_e32 v84, v85, v84
	v_max_f32_e64 v85, |v83|, |v83|
	v_max_f32_e64 v174, |v82|, |v82|
	v_max_f32_e32 v85, v174, v85
	v_max_f32_e64 v174, |v109|, |v109|
	v_max_f32_e64 v175, |v108|, |v108|
	v_max_f32_e32 v174, v175, v174
	v_max3_f32 v174, |v106|, |v107|, v174
	v_max3_f32 v84, v84, v85, v174
	v_mul_f32_e32 v84, 0x3c010204, v84
	v_lshrrev_b32_e32 v85, 23, v84
	v_and_b32_e32 v84, 0x7f800000, v84
	v_sub_u32_e32 v84, 0x7e800000, v84
	v_fmaak_f32 v80, v80, v84, 0x43000000
	v_cvt_pk_u8_f32 v80, v80, 0, 0
	v_fmaak_f32 v81, v81, v84, 0x43000000
	v_cvt_pk_u8_f32 v80, v81, 1, v80
	v_fmaak_f32 v81, v82, v84, 0x43000000
	v_cvt_pk_u8_f32 v80, v81, 2, v80
	v_fmaak_f32 v81, v83, v84, 0x43000000
	v_cvt_pk_u8_f32 v80, v81, 3, v80
	v_fmaak_f32 v81, v106, v84, 0x43000000
	v_cvt_pk_u8_f32 v81, v81, 0, 0
	v_fmaak_f32 v82, v107, v84, 0x43000000
	v_cvt_pk_u8_f32 v81, v82, 1, v81
	v_fmaak_f32 v82, v108, v84, 0x43000000
	v_cvt_pk_u8_f32 v81, v82, 2, v81
	v_fmaak_f32 v82, v109, v84, 0x43000000
	v_cvt_pk_u8_f32 v81, v82, 3, v81
	v_add_u16_e32 v82, 1, v85
	v_add_u32_e32 v106, v89, v86
	ds_read_b128 v[110:113], v94 offset:16384
	ds_read_b128 v[114:117], v94 offset:24576
	ds_read_b128 v[118:121], v95 offset:16384
	ds_read_b128 v[122:125], v95 offset:24576
	ds_read_b128 v[126:129], v96 offset:16384
	ds_read_b128 v[130:133], v96 offset:24576
	ds_read_b128 v[134:137], v97 offset:16384
	ds_read_b128 v[138:141], v97 offset:24576
	ds_read_b128 v[142:145], v98 offset:16384
	ds_read_b128 v[146:149], v98 offset:24576
	ds_read_b128 v[150:153], v99 offset:16384
	ds_read_b128 v[154:157], v99 offset:24576
	ds_read_b128 v[158:161], v100 offset:16384
	ds_read_b128 v[162:165], v100 offset:24576
	ds_read_b128 v[166:169], v101 offset:16384
	ds_read_b128 v[170:173], v101 offset:24576
	ds_write_b8 v106, v82 offset:128
	v_max_f32_e64 v82, |v73|, |v73|
	v_max_f32_e64 v83, |v72|, |v72|
	v_max_f32_e32 v82, v83, v82
	v_max_f32_e64 v83, |v75|, |v75|
	v_max_f32_e64 v84, |v74|, |v74|
	v_max_f32_e32 v83, v84, v83
	v_max_f32_e64 v84, |v79|, |v79|
	v_max_f32_e64 v85, |v78|, |v78|
	v_max_f32_e32 v84, v85, v84
	v_max3_f32 v84, |v76|, |v77|, v84
	v_max3_f32 v82, v82, v83, v84
	v_mul_f32_e32 v82, 0x3c010204, v82
	v_lshrrev_b32_e32 v83, 23, v82
	v_and_b32_e32 v82, 0x7f800000, v82
	v_sub_u32_e32 v82, 0x7e800000, v82
	v_fmaak_f32 v72, v72, v82, 0x43000000
	v_cvt_pk_u8_f32 v72, v72, 0, 0
	v_fmaak_f32 v73, v73, v82, 0x43000000
	v_cvt_pk_u8_f32 v72, v73, 1, v72
	v_fmaak_f32 v73, v74, v82, 0x43000000
	v_cvt_pk_u8_f32 v72, v73, 2, v72
	v_fmaak_f32 v73, v75, v82, 0x43000000
	v_cvt_pk_u8_f32 v72, v73, 3, v72
	v_fmaak_f32 v73, v76, v82, 0x43000000
	v_cvt_pk_u8_f32 v73, v73, 0, 0
	v_fmaak_f32 v74, v77, v82, 0x43000000
	v_cvt_pk_u8_f32 v73, v74, 1, v73
	v_fmaak_f32 v74, v78, v82, 0x43000000
	v_cvt_pk_u8_f32 v73, v74, 2, v73
	v_fmaak_f32 v74, v79, v82, 0x43000000
	v_cvt_pk_u8_f32 v73, v74, 3, v73
	ds_write2st64_b64 v102, v[80:81], v[72:73] offset1:5
	v_add_u16_e32 v72, 1, v83
	ds_write_b8 v106, v72 offset:2688
	s_setprio 1
	s_waitcnt lgkmcnt(0)
	v_mfma_f32_16x16x32_bf16 v[72:75], v[110:113], v[0:3], 0
	v_mfma_f32_16x16x32_bf16 v[76:79], v[114:117], v[0:3], 0
	v_mfma_f32_16x16x32_bf16 v[80:83], v[110:113], v[32:35], 0
	v_mfma_f32_16x16x32_bf16 v[108:111], v[114:117], v[32:35], 0
	v_mfma_f32_16x16x32_bf16 v[72:75], v[118:121], v[4:7], v[72:75]
	v_mfma_f32_16x16x32_bf16 v[76:79], v[122:125], v[4:7], v[76:79]
	v_mfma_f32_16x16x32_bf16 v[108:111], v[122:125], v[36:39], v[108:111]
	v_mfma_f32_16x16x32_bf16 v[80:83], v[118:121], v[36:39], v[80:83]
	v_mfma_f32_16x16x32_bf16 v[72:75], v[126:129], v[8:11], v[72:75]
	v_mfma_f32_16x16x32_bf16 v[76:79], v[130:133], v[8:11], v[76:79]
	v_mfma_f32_16x16x32_bf16 v[108:111], v[130:133], v[40:43], v[108:111]
	v_mfma_f32_16x16x32_bf16 v[80:83], v[126:129], v[40:43], v[80:83]
	v_mfma_f32_16x16x32_bf16 v[72:75], v[134:137], v[12:15], v[72:75]
	v_mfma_f32_16x16x32_bf16 v[76:79], v[138:141], v[12:15], v[76:79]
	v_mfma_f32_16x16x32_bf16 v[108:111], v[138:141], v[44:47], v[108:111]
	v_mfma_f32_16x16x32_bf16 v[80:83], v[134:137], v[44:47], v[80:83]
	v_mfma_f32_16x16x32_bf16 v[72:75], v[142:145], v[16:19], v[72:75]
	v_mfma_f32_16x16x32_bf16 v[76:79], v[146:149], v[16:19], v[76:79]
	v_mfma_f32_16x16x32_bf16 v[108:111], v[146:149], v[48:51], v[108:111]
	v_mfma_f32_16x16x32_bf16 v[80:83], v[142:145], v[48:51], v[80:83]
	v_mfma_f32_16x16x32_bf16 v[72:75], v[150:153], v[20:23], v[72:75]
	v_mfma_f32_16x16x32_bf16 v[76:79], v[154:157], v[20:23], v[76:79]
	v_mfma_f32_16x16x32_bf16 v[108:111], v[154:157], v[52:55], v[108:111]
	v_mfma_f32_16x16x32_bf16 v[80:83], v[150:153], v[52:55], v[80:83]
	v_mfma_f32_16x16x32_bf16 v[72:75], v[158:161], v[24:27], v[72:75]
	v_mfma_f32_16x16x32_bf16 v[76:79], v[162:165], v[24:27], v[76:79]
	v_mfma_f32_16x16x32_bf16 v[108:111], v[162:165], v[56:59], v[108:111]
	v_mfma_f32_16x16x32_bf16 v[80:83], v[158:161], v[56:59], v[80:83]
	v_mfma_f32_16x16x32_bf16 v[72:75], v[166:169], v[28:31], v[72:75]
	v_mfma_f32_16x16x32_bf16 v[76:79], v[170:173], v[28:31], v[76:79]
	v_mfma_f32_16x16x32_bf16 v[108:111], v[170:173], v[60:63], v[108:111]
	v_mfma_f32_16x16x32_bf16 v[80:83], v[166:169], v[60:63], v[80:83]
	s_setprio 0
	s_nop 3
	v_max_f32_e64 v84, |v73|, |v73|
	v_max_f32_e64 v85, |v72|, |v72|
	v_max_f32_e32 v84, v85, v84
	v_max_f32_e64 v85, |v75|, |v75|
	v_max_f32_e64 v107, |v74|, |v74|
	v_max_f32_e32 v85, v107, v85
	v_max_f32_e64 v107, |v79|, |v79|
	v_max_f32_e64 v112, |v78|, |v78|
	v_max_f32_e32 v107, v112, v107
	v_max3_f32 v107, |v76|, |v77|, v107
	v_max3_f32 v84, v84, v85, v107
	v_mul_f32_e32 v84, 0x3c010204, v84
	v_lshrrev_b32_e32 v85, 23, v84
	v_and_b32_e32 v84, 0x7f800000, v84
	v_sub_u32_e32 v84, 0x7e800000, v84
	v_fmaak_f32 v72, v72, v84, 0x43000000
	v_cvt_pk_u8_f32 v72, v72, 0, 0
	v_fmaak_f32 v73, v73, v84, 0x43000000
	v_cvt_pk_u8_f32 v72, v73, 1, v72
	v_fmaak_f32 v73, v74, v84, 0x43000000
	v_cvt_pk_u8_f32 v72, v73, 2, v72
	v_fmaak_f32 v73, v75, v84, 0x43000000
	v_cvt_pk_u8_f32 v72, v73, 3, v72
	v_fmaak_f32 v73, v76, v84, 0x43000000
	v_cvt_pk_u8_f32 v73, v73, 0, 0
	v_fmaak_f32 v74, v77, v84, 0x43000000
	v_cvt_pk_u8_f32 v73, v74, 1, v73
	v_fmaak_f32 v74, v78, v84, 0x43000000
	v_cvt_pk_u8_f32 v73, v74, 2, v73
	v_fmaak_f32 v74, v79, v84, 0x43000000
	v_cvt_pk_u8_f32 v73, v74, 3, v73
	v_add_u16_e32 v74, 1, v85
	ds_write_b8 v106, v74 offset:132
	v_max_f32_e64 v74, |v81|, |v81|
	v_max_f32_e64 v75, |v80|, |v80|
	v_max_f32_e32 v74, v75, v74
	v_max_f32_e64 v75, |v83|, |v83|
	v_max_f32_e64 v76, |v82|, |v82|
	v_max_f32_e32 v75, v76, v75
	v_max_f32_e64 v76, |v111|, |v111|
	v_max_f32_e64 v77, |v110|, |v110|
	v_max_f32_e32 v76, v77, v76
	v_max3_f32 v76, |v108|, |v109|, v76
	v_max3_f32 v74, v74, v75, v76
	v_mul_f32_e32 v74, 0x3c010204, v74
	v_lshrrev_b32_e32 v76, 23, v74
	v_and_b32_e32 v74, 0x7f800000, v74
	v_sub_u32_e32 v75, 0x7e800000, v74
	v_fmaak_f32 v74, v80, v75, 0x43000000
	v_cvt_pk_u8_f32 v74, v74, 0, 0
	v_fmaak_f32 v77, v81, v75, 0x43000000
	v_cvt_pk_u8_f32 v74, v77, 1, v74
	v_fmaak_f32 v77, v82, v75, 0x43000000
	v_cvt_pk_u8_f32 v74, v77, 2, v74
	v_fmaak_f32 v77, v83, v75, 0x43000000
	v_cvt_pk_u8_f32 v74, v77, 3, v74
	v_fmaak_f32 v77, v108, v75, 0x43000000
	v_cvt_pk_u8_f32 v77, v77, 0, 0
	v_fmaak_f32 v78, v109, v75, 0x43000000
	v_cvt_pk_u8_f32 v77, v78, 1, v77
	v_fmaak_f32 v78, v110, v75, 0x43000000
	v_cvt_pk_u8_f32 v77, v78, 2, v77
	v_fmaak_f32 v75, v111, v75, 0x43000000
	v_cvt_pk_u8_f32 v75, v75, 3, v77
	v_add_u32_e32 v107, 32, v102
	s_add_u32 s6, s16, 0x10000
	ds_write2st64_b64 v107, v[72:73], v[74:75] offset1:5
	v_add_u16_e32 v72, 1, v76
	s_addc_u32 s7, s17, 0
	s_mov_b32 m0, s30
	ds_write_b8 v106, v72 offset:2692
	v_lshl_add_u64 v[72:73], s[6:7], 0, v[176:177]
	s_waitcnt vmcnt(0)
	s_barrier
	global_load_lds_dwordx4 v[72:73], off
	v_lshl_add_u64 v[72:73], s[6:7], 0, v[64:65]
	s_add_u32 s6, s16, 0x14000
	s_mov_b32 m0, s18
	s_addc_u32 s7, s17, 0
	global_load_lds_dwordx4 v[72:73], off
	v_lshl_add_u64 v[72:73], s[6:7], 0, v[176:177]
	s_mov_b32 m0, s19
	s_nop 0
	global_load_lds_dwordx4 v[72:73], off
	v_lshl_add_u64 v[72:73], s[6:7], 0, v[64:65]
	s_mov_b32 m0, s31
	s_nop 0
	global_load_lds_dwordx4 v[72:73], off
	ds_read_b128 v[72:75], v94 offset:32768
	ds_read_b128 v[76:79], v94 offset:40960
	ds_read_b128 v[80:83], v95 offset:32768
	ds_read_b128 v[108:111], v95 offset:40960
	ds_read_b128 v[112:115], v96 offset:32768
	ds_read_b128 v[116:119], v96 offset:40960
	ds_read_b128 v[120:123], v97 offset:32768
	ds_read_b128 v[124:127], v97 offset:40960
	ds_read_b128 v[128:131], v98 offset:32768
	ds_read_b128 v[132:135], v98 offset:40960
	ds_read_b128 v[136:139], v99 offset:32768
	ds_read_b128 v[140:143], v99 offset:40960
	ds_read_b128 v[144:147], v100 offset:32768
	ds_read_b128 v[148:151], v100 offset:40960
	ds_read_b128 v[152:155], v101 offset:32768
	ds_read_b128 v[156:159], v101 offset:40960
	s_setprio 1
	s_waitcnt lgkmcnt(0)
	v_mfma_f32_16x16x32_bf16 v[160:163], v[72:75], v[0:3], 0
	v_mfma_f32_16x16x32_bf16 v[164:167], v[76:79], v[0:3], 0
	v_mfma_f32_16x16x32_bf16 v[72:75], v[72:75], v[32:35], 0
	v_mfma_f32_16x16x32_bf16 v[76:79], v[76:79], v[32:35], 0
	v_mfma_f32_16x16x32_bf16 v[164:167], v[108:111], v[4:7], v[164:167]
	v_mfma_f32_16x16x32_bf16 v[72:75], v[80:83], v[36:39], v[72:75]
	v_mfma_f32_16x16x32_bf16 v[76:79], v[108:111], v[36:39], v[76:79]
	v_mfma_f32_16x16x32_bf16 v[160:163], v[80:83], v[4:7], v[160:163]
	v_mfma_f32_16x16x32_bf16 v[108:111], v[116:119], v[8:11], v[164:167]
	v_mfma_f32_16x16x32_bf16 v[72:75], v[112:115], v[40:43], v[72:75]
	v_mfma_f32_16x16x32_bf16 v[76:79], v[116:119], v[40:43], v[76:79]
	v_mfma_f32_16x16x32_bf16 v[80:83], v[112:115], v[8:11], v[160:163]
	v_mfma_f32_16x16x32_bf16 v[108:111], v[124:127], v[12:15], v[108:111]
	v_mfma_f32_16x16x32_bf16 v[72:75], v[120:123], v[44:47], v[72:75]
	v_mfma_f32_16x16x32_bf16 v[76:79], v[124:127], v[44:47], v[76:79]
	v_mfma_f32_16x16x32_bf16 v[80:83], v[120:123], v[12:15], v[80:83]
	v_mfma_f32_16x16x32_bf16 v[108:111], v[132:135], v[16:19], v[108:111]
	v_mfma_f32_16x16x32_bf16 v[72:75], v[128:131], v[48:51], v[72:75]
	v_mfma_f32_16x16x32_bf16 v[76:79], v[132:135], v[48:51], v[76:79]
	v_mfma_f32_16x16x32_bf16 v[80:83], v[128:131], v[16:19], v[80:83]
	v_mfma_f32_16x16x32_bf16 v[108:111], v[140:143], v[20:23], v[108:111]
	v_mfma_f32_16x16x32_bf16 v[72:75], v[136:139], v[52:55], v[72:75]
	v_mfma_f32_16x16x32_bf16 v[76:79], v[140:143], v[52:55], v[76:79]
	v_mfma_f32_16x16x32_bf16 v[80:83], v[136:139], v[20:23], v[80:83]
	v_mfma_f32_16x16x32_bf16 v[108:111], v[148:151], v[24:27], v[108:111]
	v_mfma_f32_16x16x32_bf16 v[72:75], v[144:147], v[56:59], v[72:75]
	v_mfma_f32_16x16x32_bf16 v[76:79], v[148:151], v[56:59], v[76:79]
	v_mfma_f32_16x16x32_bf16 v[80:83], v[144:147], v[24:27], v[80:83]
	v_mfma_f32_16x16x32_bf16 v[108:111], v[156:159], v[28:31], v[108:111]
	v_mfma_f32_16x16x32_bf16 v[72:75], v[152:155], v[60:63], v[72:75]
	v_mfma_f32_16x16x32_bf16 v[76:79], v[156:159], v[60:63], v[76:79]
	v_mfma_f32_16x16x32_bf16 v[80:83], v[152:155], v[28:31], v[80:83]
	s_setprio 0
	s_nop 6
	v_max_f32_e64 v84, |v81|, |v81|
	v_max_f32_e64 v85, |v80|, |v80|
	v_max_f32_e32 v84, v85, v84
	v_max_f32_e64 v85, |v83|, |v83|
	v_max_f32_e64 v178, |v82|, |v82|
	v_max_f32_e32 v85, v178, v85
	v_max_f32_e64 v178, |v111|, |v111|
	v_max_f32_e64 v179, |v110|, |v110|
	v_max_f32_e32 v178, v179, v178
	v_max3_f32 v178, |v108|, |v109|, v178
	v_max3_f32 v84, v84, v85, v178
	v_mul_f32_e32 v84, 0x3c010204, v84
	v_lshrrev_b32_e32 v85, 23, v84
	v_and_b32_e32 v84, 0x7f800000, v84
	v_sub_u32_e32 v84, 0x7e800000, v84
	v_fmaak_f32 v80, v80, v84, 0x43000000
	v_cvt_pk_u8_f32 v80, v80, 0, 0
	v_fmaak_f32 v81, v81, v84, 0x43000000
	v_cvt_pk_u8_f32 v80, v81, 1, v80
	v_fmaak_f32 v81, v82, v84, 0x43000000
	v_cvt_pk_u8_f32 v80, v81, 2, v80
	v_fmaak_f32 v81, v83, v84, 0x43000000
	v_cvt_pk_u8_f32 v80, v81, 3, v80
	v_fmaak_f32 v81, v108, v84, 0x43000000
	v_cvt_pk_u8_f32 v81, v81, 0, 0
	v_fmaak_f32 v82, v109, v84, 0x43000000
	v_cvt_pk_u8_f32 v81, v82, 1, v81
	v_fmaak_f32 v82, v110, v84, 0x43000000
	v_cvt_pk_u8_f32 v81, v82, 2, v81
	v_fmaak_f32 v82, v111, v84, 0x43000000
	v_cvt_pk_u8_f32 v81, v82, 3, v81
	v_add_u16_e32 v82, 1, v85
	ds_read_b128 v[112:115], v94 offset:49152
	ds_read_b128 v[116:119], v94 offset:57344
	ds_read_b128 v[120:123], v95 offset:49152
	ds_read_b128 v[124:127], v95 offset:57344
	ds_read_b128 v[128:131], v96 offset:49152
	ds_read_b128 v[132:135], v96 offset:57344
	ds_read_b128 v[136:139], v97 offset:49152
	ds_read_b128 v[140:143], v97 offset:57344
	ds_read_b128 v[144:147], v98 offset:49152
	ds_read_b128 v[148:151], v98 offset:57344
	ds_read_b128 v[152:155], v99 offset:49152
	ds_read_b128 v[156:159], v99 offset:57344
	ds_read_b128 v[160:163], v100 offset:49152
	ds_read_b128 v[164:167], v100 offset:57344
	ds_read_b128 v[168:171], v101 offset:49152
	ds_read_b128 v[172:175], v101 offset:57344
	ds_write_b8 v106, v82 offset:136
	v_max_f32_e64 v82, |v73|, |v73|
	v_max_f32_e64 v83, |v72|, |v72|
	v_max_f32_e32 v82, v83, v82
	v_max_f32_e64 v83, |v75|, |v75|
	v_max_f32_e64 v84, |v74|, |v74|
	v_max_f32_e32 v83, v84, v83
	v_max_f32_e64 v84, |v79|, |v79|
	v_max_f32_e64 v85, |v78|, |v78|
	v_max_f32_e32 v84, v85, v84
	v_max3_f32 v84, |v76|, |v77|, v84
	v_max3_f32 v82, v82, v83, v84
	v_mul_f32_e32 v82, 0x3c010204, v82
	v_lshrrev_b32_e32 v83, 23, v82
	v_and_b32_e32 v82, 0x7f800000, v82
	v_sub_u32_e32 v82, 0x7e800000, v82
	v_fmaak_f32 v72, v72, v82, 0x43000000
	v_cvt_pk_u8_f32 v72, v72, 0, 0
	v_fmaak_f32 v73, v73, v82, 0x43000000
	v_cvt_pk_u8_f32 v72, v73, 1, v72
	v_fmaak_f32 v73, v74, v82, 0x43000000
	v_cvt_pk_u8_f32 v72, v73, 2, v72
	v_fmaak_f32 v73, v75, v82, 0x43000000
	v_cvt_pk_u8_f32 v72, v73, 3, v72
	v_fmaak_f32 v73, v76, v82, 0x43000000
	v_cvt_pk_u8_f32 v73, v73, 0, 0
	v_fmaak_f32 v74, v77, v82, 0x43000000
	v_cvt_pk_u8_f32 v73, v74, 1, v73
	v_fmaak_f32 v74, v78, v82, 0x43000000
	v_cvt_pk_u8_f32 v73, v74, 2, v73
	v_fmaak_f32 v74, v79, v82, 0x43000000
	v_cvt_pk_u8_f32 v73, v74, 3, v73
	v_add_u32_e32 v108, 64, v102
	ds_write2st64_b64 v108, v[80:81], v[72:73] offset1:5
	v_add_u16_e32 v72, 1, v83
	ds_write_b8 v106, v72 offset:2696
	s_setprio 1
	s_waitcnt lgkmcnt(0)
	v_mfma_f32_16x16x32_bf16 v[72:75], v[112:115], v[0:3], 0
	v_mfma_f32_16x16x32_bf16 v[76:79], v[116:119], v[0:3], 0
	v_mfma_f32_16x16x32_bf16 v[80:83], v[112:115], v[32:35], 0
	v_mfma_f32_16x16x32_bf16 v[110:113], v[116:119], v[32:35], 0
	v_mfma_f32_16x16x32_bf16 v[72:75], v[120:123], v[4:7], v[72:75]
	v_mfma_f32_16x16x32_bf16 v[76:79], v[124:127], v[4:7], v[76:79]
	v_mfma_f32_16x16x32_bf16 v[80:83], v[120:123], v[36:39], v[80:83]
	v_mfma_f32_16x16x32_bf16 v[110:113], v[124:127], v[36:39], v[110:113]
	v_mfma_f32_16x16x32_bf16 v[72:75], v[128:131], v[8:11], v[72:75]
	v_mfma_f32_16x16x32_bf16 v[76:79], v[132:135], v[8:11], v[76:79]
	v_mfma_f32_16x16x32_bf16 v[80:83], v[128:131], v[40:43], v[80:83]
	v_mfma_f32_16x16x32_bf16 v[110:113], v[132:135], v[40:43], v[110:113]
	v_mfma_f32_16x16x32_bf16 v[72:75], v[136:139], v[12:15], v[72:75]
	v_mfma_f32_16x16x32_bf16 v[76:79], v[140:143], v[12:15], v[76:79]
	v_mfma_f32_16x16x32_bf16 v[80:83], v[136:139], v[44:47], v[80:83]
	v_mfma_f32_16x16x32_bf16 v[110:113], v[140:143], v[44:47], v[110:113]
	v_mfma_f32_16x16x32_bf16 v[72:75], v[144:147], v[16:19], v[72:75]
	v_mfma_f32_16x16x32_bf16 v[76:79], v[148:151], v[16:19], v[76:79]
	v_mfma_f32_16x16x32_bf16 v[80:83], v[144:147], v[48:51], v[80:83]
	v_mfma_f32_16x16x32_bf16 v[110:113], v[148:151], v[48:51], v[110:113]
	v_mfma_f32_16x16x32_bf16 v[72:75], v[152:155], v[20:23], v[72:75]
	v_mfma_f32_16x16x32_bf16 v[76:79], v[156:159], v[20:23], v[76:79]
	v_mfma_f32_16x16x32_bf16 v[80:83], v[152:155], v[52:55], v[80:83]
	v_mfma_f32_16x16x32_bf16 v[110:113], v[156:159], v[52:55], v[110:113]
	v_mfma_f32_16x16x32_bf16 v[72:75], v[160:163], v[24:27], v[72:75]
	v_mfma_f32_16x16x32_bf16 v[76:79], v[164:167], v[24:27], v[76:79]
	v_mfma_f32_16x16x32_bf16 v[80:83], v[160:163], v[56:59], v[80:83]
	v_mfma_f32_16x16x32_bf16 v[110:113], v[164:167], v[56:59], v[110:113]
	v_mfma_f32_16x16x32_bf16 v[72:75], v[168:171], v[28:31], v[72:75]
	v_mfma_f32_16x16x32_bf16 v[76:79], v[172:175], v[28:31], v[76:79]
	v_mfma_f32_16x16x32_bf16 v[80:83], v[168:171], v[60:63], v[80:83]
	v_mfma_f32_16x16x32_bf16 v[110:113], v[172:175], v[60:63], v[110:113]
	s_setprio 0
	s_nop 3
	v_max_f32_e64 v84, |v73|, |v73|
	v_max_f32_e64 v85, |v72|, |v72|
	v_max_f32_e32 v84, v85, v84
	v_max_f32_e64 v85, |v75|, |v75|
	v_max_f32_e64 v109, |v74|, |v74|
	v_max_f32_e32 v85, v109, v85
	v_max_f32_e64 v109, |v79|, |v79|
	v_max_f32_e64 v114, |v78|, |v78|
	v_max_f32_e32 v109, v114, v109
	v_max3_f32 v109, |v76|, |v77|, v109
	v_max3_f32 v84, v84, v85, v109
	v_mul_f32_e32 v84, 0x3c010204, v84
	v_lshrrev_b32_e32 v85, 23, v84
	v_and_b32_e32 v84, 0x7f800000, v84
	v_sub_u32_e32 v84, 0x7e800000, v84
	v_fmaak_f32 v72, v72, v84, 0x43000000
	v_cvt_pk_u8_f32 v72, v72, 0, 0
	v_fmaak_f32 v73, v73, v84, 0x43000000
	v_cvt_pk_u8_f32 v72, v73, 1, v72
	v_fmaak_f32 v73, v74, v84, 0x43000000
	v_cvt_pk_u8_f32 v72, v73, 2, v72
	v_fmaak_f32 v73, v75, v84, 0x43000000
	v_cvt_pk_u8_f32 v72, v73, 3, v72
	v_fmaak_f32 v73, v76, v84, 0x43000000
	v_cvt_pk_u8_f32 v73, v73, 0, 0
	v_fmaak_f32 v74, v77, v84, 0x43000000
	v_cvt_pk_u8_f32 v73, v74, 1, v73
	v_fmaak_f32 v74, v78, v84, 0x43000000
	v_cvt_pk_u8_f32 v73, v74, 2, v73
	v_fmaak_f32 v74, v79, v84, 0x43000000
	v_cvt_pk_u8_f32 v73, v74, 3, v73
	v_add_u16_e32 v74, 1, v85
	ds_write_b8 v106, v74 offset:140
	v_max_f32_e64 v74, |v81|, |v81|
	v_max_f32_e64 v75, |v80|, |v80|
	v_max_f32_e32 v74, v75, v74
	v_max_f32_e64 v75, |v83|, |v83|
	v_max_f32_e64 v76, |v82|, |v82|
	v_max_f32_e32 v75, v76, v75
	v_max_f32_e64 v76, |v113|, |v113|
	v_max_f32_e64 v77, |v112|, |v112|
	v_max_f32_e32 v76, v77, v76
	v_max3_f32 v76, |v110|, |v111|, v76
	v_max3_f32 v74, v74, v75, v76
	v_mul_f32_e32 v74, 0x3c010204, v74
	v_lshrrev_b32_e32 v76, 23, v74
	v_and_b32_e32 v74, 0x7f800000, v74
	v_sub_u32_e32 v75, 0x7e800000, v74
	v_fmaak_f32 v74, v80, v75, 0x43000000
	v_cvt_pk_u8_f32 v74, v74, 0, 0
	v_fmaak_f32 v77, v81, v75, 0x43000000
	v_cvt_pk_u8_f32 v74, v77, 1, v74
	v_fmaak_f32 v77, v82, v75, 0x43000000
	v_cvt_pk_u8_f32 v74, v77, 2, v74
	v_fmaak_f32 v77, v83, v75, 0x43000000
	v_cvt_pk_u8_f32 v74, v77, 3, v74
	v_fmaak_f32 v77, v110, v75, 0x43000000
	v_cvt_pk_u8_f32 v77, v77, 0, 0
	v_fmaak_f32 v78, v111, v75, 0x43000000
	v_cvt_pk_u8_f32 v77, v78, 1, v77
	v_fmaak_f32 v78, v112, v75, 0x43000000
	v_cvt_pk_u8_f32 v77, v78, 2, v77
	v_fmaak_f32 v75, v113, v75, 0x43000000
	v_cvt_pk_u8_f32 v75, v75, 3, v77
	v_add_u32_e32 v109, 0x60, v102
	ds_write2st64_b64 v109, v[72:73], v[74:75] offset1:5
	v_add_u16_e32 v72, 1, v76
	ds_write_b8 v106, v72 offset:2700
	ds_read_b128 v[76:79], v103
	ds_read_b128 v[80:83], v103 offset:1280
	s_add_i32 s8, s40, s29
	v_add_u32_e32 v74, s8, v90
	v_mad_i64_i32 v[72:73], s[6:7], v74, s50, v[68:69]
	v_add_u32_e32 v75, s8, v91
	s_waitcnt lgkmcnt(0)
	s_cmp_lt_u32 s28, 2
	s_cbranch_scc1 .Ledc_nt0
	global_store_dwordx4 v[72:73], v[76:79], off
	s_branch .Ledc_dn0
.Ledc_nt0:
	global_store_dwordx4 v[72:73], v[76:79], off nt
.Ledc_dn0:
	v_mad_i64_i32 v[72:73], s[6:7], v75, s50, v[68:69]
	s_cmp_lt_u32 s28, 2
	s_cbranch_scc1 .Ledc_nt1
	global_store_dwordx4 v[72:73], v[80:83], off
	s_branch .Ledc_dn1
.Ledc_nt1:
	global_store_dwordx4 v[72:73], v[80:83], off nt
.Ledc_dn1:
	ds_read_b128 v[78:81], v103 offset:2560
	ds_read_b128 v[82:85], v103 offset:3840
	v_add_u32_e32 v76, s8, v92
	v_mad_i64_i32 v[72:73], s[6:7], v76, s50, v[68:69]
	v_add_u32_e32 v77, s8, v93
	s_waitcnt lgkmcnt(0)
	s_cmp_lt_u32 s28, 2
	s_cbranch_scc1 .Ledc_nt2
	global_store_dwordx4 v[72:73], v[78:81], off
	s_branch .Ledc_dn2
.Ledc_nt2:
	global_store_dwordx4 v[72:73], v[78:81], off nt
.Ledc_dn2:
	v_mad_i64_i32 v[72:73], s[6:7], v77, s50, v[68:69]
	s_nop 0
	v_add_u32_e32 v78, s40, v88
	s_cmp_lt_u32 s28, 2
	s_cbranch_scc1 .Ledc_nt3
	global_store_dwordx4 v[72:73], v[82:85], off
	s_branch .Ledc_dn3
.Ledc_nt3:
	global_store_dwordx4 v[72:73], v[82:85], off nt
.Ledc_dn3:
	s_and_saveexec_b64 s[6:7], s[4:5]
	s_xor_b64 s[6:7], exec, s[6:7]
	v_mad_i64_i32 v[72:73], s[8:9], v78, s50, 0
	s_andn2_saveexec_b64 s[6:7], s[6:7]
	s_cbranch_execz .LBB0_1286
	ds_read_b128 v[80:83], v104 offset:128
	v_mov_b64_e32 v[84:85], s[10:11]
	v_mad_i64_i32 v[72:73], s[8:9], v78, s50, 0
	v_mad_i64_i32 v[78:79], s[8:9], v78, s50, v[84:85]
	s_waitcnt lgkmcnt(0)
	s_cmp_lt_u32 s28, 2
	s_cbranch_scc1 .Ledc_nt4
	global_store_dwordx4 v[78:79], v[80:83], off offset:1024
	s_branch .Ledc_dn4
.Ledc_nt4:
	global_store_dwordx4 v[78:79], v[80:83], off offset:1024 nt
.Ledc_dn4:
.LBB0_1286:
	s_or_b64 exec, exec, s[6:7]
	s_nop 0
	v_mad_i64_i32 v[80:81], s[6:7], v74, s50, 0
	v_mad_i64_i32 v[78:79], s[6:7], v75, s50, 0
	v_mad_i64_i32 v[82:83], s[6:7], v76, s50, 0
	v_mad_i64_i32 v[74:75], s[6:7], v77, s50, 0
	s_mov_b64 s[6:7], 0x2e2c2c10
	s_nop 0
	v_lshl_add_u64 v[72:73], v[72:73], 0, s[6:7]
	v_lshl_add_u64 v[74:75], v[70:71], 0, v[74:75]
	v_lshl_add_u64 v[76:77], v[70:71], 0, v[82:83]
	v_lshl_add_u64 v[78:79], v[70:71], 0, v[78:79]
	v_lshl_add_u64 v[80:81], v[70:71], 0, v[80:81]
	s_mov_b32 s40, 2
	s_branch .LBB0_1288

.LBB0_1290:
	ds_read_b128 v[82:85], v94 offset:32768
	ds_read_b128 v[110:113], v94 offset:40960
	ds_read_b128 v[114:117], v95 offset:32768
	ds_read_b128 v[118:121], v95 offset:40960
	ds_read_b128 v[122:125], v96 offset:32768
	ds_read_b128 v[126:129], v96 offset:40960
	ds_read_b128 v[130:133], v97 offset:32768
	ds_read_b128 v[134:137], v97 offset:40960
	ds_read_b128 v[138:141], v98 offset:32768
	ds_read_b128 v[142:145], v98 offset:40960
	ds_read_b128 v[146:149], v99 offset:32768
	ds_read_b128 v[150:153], v99 offset:40960
	ds_read_b128 v[154:157], v100 offset:32768
	ds_read_b128 v[158:161], v100 offset:40960
	ds_read_b128 v[162:165], v101 offset:32768
	ds_read_b128 v[166:169], v101 offset:40960
	s_setprio 1
	s_waitcnt lgkmcnt(0)
	v_mfma_f32_16x16x32_bf16 v[170:173], v[82:85], v[0:3], 0
	v_mfma_f32_16x16x32_bf16 v[178:181], v[110:113], v[0:3], 0
	v_mfma_f32_16x16x32_bf16 v[82:85], v[82:85], v[32:35], 0
	v_mfma_f32_16x16x32_bf16 v[110:113], v[110:113], v[32:35], 0
	v_mfma_f32_16x16x32_bf16 v[170:173], v[114:117], v[4:7], v[170:173]
	v_mfma_f32_16x16x32_bf16 v[178:181], v[118:121], v[4:7], v[178:181]
	v_mfma_f32_16x16x32_bf16 v[82:85], v[114:117], v[36:39], v[82:85]
	v_mfma_f32_16x16x32_bf16 v[110:113], v[118:121], v[36:39], v[110:113]
	v_mfma_f32_16x16x32_bf16 v[114:117], v[122:125], v[8:11], v[170:173]
	v_mfma_f32_16x16x32_bf16 v[118:121], v[126:129], v[8:11], v[178:181]
	v_mfma_f32_16x16x32_bf16 v[82:85], v[122:125], v[40:43], v[82:85]
	v_mfma_f32_16x16x32_bf16 v[110:113], v[126:129], v[40:43], v[110:113]
	v_mfma_f32_16x16x32_bf16 v[114:117], v[130:133], v[12:15], v[114:117]
	v_mfma_f32_16x16x32_bf16 v[118:121], v[134:137], v[12:15], v[118:121]
	v_mfma_f32_16x16x32_bf16 v[82:85], v[130:133], v[44:47], v[82:85]
	v_mfma_f32_16x16x32_bf16 v[110:113], v[134:137], v[44:47], v[110:113]
	v_mfma_f32_16x16x32_bf16 v[114:117], v[138:141], v[16:19], v[114:117]
	v_mfma_f32_16x16x32_bf16 v[118:121], v[142:145], v[16:19], v[118:121]
	v_mfma_f32_16x16x32_bf16 v[82:85], v[138:141], v[48:51], v[82:85]
	v_mfma_f32_16x16x32_bf16 v[110:113], v[142:145], v[48:51], v[110:113]
	v_mfma_f32_16x16x32_bf16 v[114:117], v[146:149], v[20:23], v[114:117]
	v_mfma_f32_16x16x32_bf16 v[118:121], v[150:153], v[20:23], v[118:121]
	v_mfma_f32_16x16x32_bf16 v[82:85], v[146:149], v[52:55], v[82:85]
	v_mfma_f32_16x16x32_bf16 v[110:113], v[150:153], v[52:55], v[110:113]
	v_mfma_f32_16x16x32_bf16 v[114:117], v[154:157], v[24:27], v[114:117]
	v_mfma_f32_16x16x32_bf16 v[118:121], v[158:161], v[24:27], v[118:121]
	v_mfma_f32_16x16x32_bf16 v[82:85], v[154:157], v[56:59], v[82:85]
	v_mfma_f32_16x16x32_bf16 v[110:113], v[158:161], v[56:59], v[110:113]
	v_mfma_f32_16x16x32_bf16 v[114:117], v[162:165], v[28:31], v[114:117]
	v_mfma_f32_16x16x32_bf16 v[118:121], v[166:169], v[28:31], v[118:121]
	v_mfma_f32_16x16x32_bf16 v[82:85], v[162:165], v[60:63], v[82:85]
	v_mfma_f32_16x16x32_bf16 v[110:113], v[166:169], v[60:63], v[110:113]
	s_setprio 0
	s_nop 3
	v_max_f32_e64 v174, |v115|, |v115|
	v_max_f32_e64 v175, |v114|, |v114|
	v_max_f32_e32 v174, v175, v174
	v_max_f32_e64 v175, |v117|, |v117|
	v_max_f32_e64 v190, |v116|, |v116|
	v_max_f32_e32 v175, v190, v175
	v_max_f32_e64 v190, |v121|, |v121|
	v_max_f32_e64 v191, |v120|, |v120|
	v_max_f32_e32 v190, v191, v190
	v_max3_f32 v190, |v118|, |v119|, v190
	v_max3_f32 v174, v174, v175, v190
	v_mul_f32_e32 v174, 0x3c010204, v174
	v_lshrrev_b32_e32 v175, 23, v174
	v_and_b32_e32 v174, 0x7f800000, v174
	v_sub_u32_e32 v174, 0x7e800000, v174
	v_fmaak_f32 v114, v114, v174, 0x43000000
	v_cvt_pk_u8_f32 v114, v114, 0, 0
	v_fmaak_f32 v115, v115, v174, 0x43000000
	v_cvt_pk_u8_f32 v114, v115, 1, v114
	v_fmaak_f32 v115, v116, v174, 0x43000000
	v_cvt_pk_u8_f32 v114, v115, 2, v114
	v_fmaak_f32 v115, v117, v174, 0x43000000
	v_cvt_pk_u8_f32 v114, v115, 3, v114
	v_fmaak_f32 v115, v118, v174, 0x43000000
	v_cvt_pk_u8_f32 v115, v115, 0, 0
	v_fmaak_f32 v116, v119, v174, 0x43000000
	v_cvt_pk_u8_f32 v115, v116, 1, v115
	v_fmaak_f32 v116, v120, v174, 0x43000000
	v_cvt_pk_u8_f32 v115, v116, 2, v115
	v_fmaak_f32 v116, v121, v174, 0x43000000
	v_cvt_pk_u8_f32 v115, v116, 3, v115
	v_add_u16_e32 v116, 1, v175
	ds_read_b128 v[122:125], v94 offset:49152
	ds_read_b128 v[126:129], v94 offset:57344
	ds_read_b128 v[130:133], v95 offset:49152
	ds_read_b128 v[134:137], v95 offset:57344
	ds_read_b128 v[138:141], v96 offset:49152
	ds_read_b128 v[142:145], v96 offset:57344
	ds_read_b128 v[146:149], v97 offset:49152
	ds_read_b128 v[150:153], v97 offset:57344
	ds_read_b128 v[154:157], v98 offset:49152
	ds_read_b128 v[158:161], v98 offset:57344
	ds_read_b128 v[162:165], v99 offset:49152
	ds_read_b128 v[166:169], v99 offset:57344
	ds_read_b128 v[170:173], v100 offset:49152
	ds_read_b128 v[178:181], v100 offset:57344
	ds_read_b128 v[182:185], v101 offset:49152
	ds_read_b128 v[186:189], v101 offset:57344
	ds_write_b8 v106, v116 offset:136
	v_max_f32_e64 v116, |v83|, |v83|
	v_max_f32_e64 v117, |v82|, |v82|
	v_max_f32_e32 v116, v117, v116
	v_max_f32_e64 v117, |v85|, |v85|
	v_max_f32_e64 v118, |v84|, |v84|
	v_max_f32_e32 v117, v118, v117
	v_max_f32_e64 v118, |v113|, |v113|
	v_max_f32_e64 v119, |v112|, |v112|
	v_max_f32_e32 v118, v119, v118
	v_max3_f32 v118, |v110|, |v111|, v118
	v_max3_f32 v116, v116, v117, v118
	v_mul_f32_e32 v116, 0x3c010204, v116
	v_lshrrev_b32_e32 v117, 23, v116
	v_and_b32_e32 v116, 0x7f800000, v116
	v_sub_u32_e32 v116, 0x7e800000, v116
	v_fmaak_f32 v82, v82, v116, 0x43000000
	v_cvt_pk_u8_f32 v82, v82, 0, 0
	v_fmaak_f32 v83, v83, v116, 0x43000000
	v_cvt_pk_u8_f32 v82, v83, 1, v82
	v_fmaak_f32 v83, v84, v116, 0x43000000
	v_cvt_pk_u8_f32 v82, v83, 2, v82
	v_fmaak_f32 v83, v85, v116, 0x43000000
	v_cvt_pk_u8_f32 v82, v83, 3, v82
	v_fmaak_f32 v83, v110, v116, 0x43000000
	v_cvt_pk_u8_f32 v83, v83, 0, 0
	v_fmaak_f32 v84, v111, v116, 0x43000000
	v_cvt_pk_u8_f32 v83, v84, 1, v83
	v_fmaak_f32 v84, v112, v116, 0x43000000
	v_cvt_pk_u8_f32 v83, v84, 2, v83
	v_fmaak_f32 v84, v113, v116, 0x43000000
	v_cvt_pk_u8_f32 v83, v84, 3, v83
	ds_write2st64_b64 v108, v[114:115], v[82:83] offset1:5
	v_add_u16_e32 v82, 1, v117
	ds_write_b8 v106, v82 offset:2696
	s_setprio 1
	s_waitcnt lgkmcnt(0)
	v_mfma_f32_16x16x32_bf16 v[82:85], v[122:125], v[0:3], 0
	v_mfma_f32_16x16x32_bf16 v[110:113], v[126:129], v[0:3], 0
	v_mfma_f32_16x16x32_bf16 v[114:117], v[122:125], v[32:35], 0
	v_mfma_f32_16x16x32_bf16 v[118:121], v[126:129], v[32:35], 0
	v_mfma_f32_16x16x32_bf16 v[82:85], v[130:133], v[4:7], v[82:85]
	v_mfma_f32_16x16x32_bf16 v[110:113], v[134:137], v[4:7], v[110:113]
	v_mfma_f32_16x16x32_bf16 v[114:117], v[130:133], v[36:39], v[114:117]
	v_mfma_f32_16x16x32_bf16 v[118:121], v[134:137], v[36:39], v[118:121]
	v_mfma_f32_16x16x32_bf16 v[82:85], v[138:141], v[8:11], v[82:85]
	v_mfma_f32_16x16x32_bf16 v[110:113], v[142:145], v[8:11], v[110:113]
	v_mfma_f32_16x16x32_bf16 v[114:117], v[138:141], v[40:43], v[114:117]
	v_mfma_f32_16x16x32_bf16 v[118:121], v[142:145], v[40:43], v[118:121]
	v_mfma_f32_16x16x32_bf16 v[82:85], v[146:149], v[12:15], v[82:85]
	v_mfma_f32_16x16x32_bf16 v[110:113], v[150:153], v[12:15], v[110:113]
	v_mfma_f32_16x16x32_bf16 v[114:117], v[146:149], v[44:47], v[114:117]
	v_mfma_f32_16x16x32_bf16 v[118:121], v[150:153], v[44:47], v[118:121]
	v_mfma_f32_16x16x32_bf16 v[82:85], v[154:157], v[16:19], v[82:85]
	v_mfma_f32_16x16x32_bf16 v[110:113], v[158:161], v[16:19], v[110:113]
	v_mfma_f32_16x16x32_bf16 v[114:117], v[154:157], v[48:51], v[114:117]
	v_mfma_f32_16x16x32_bf16 v[118:121], v[158:161], v[48:51], v[118:121]
	v_mfma_f32_16x16x32_bf16 v[82:85], v[162:165], v[20:23], v[82:85]
	v_mfma_f32_16x16x32_bf16 v[110:113], v[166:169], v[20:23], v[110:113]
	v_mfma_f32_16x16x32_bf16 v[114:117], v[162:165], v[52:55], v[114:117]
	v_mfma_f32_16x16x32_bf16 v[118:121], v[166:169], v[52:55], v[118:121]
	v_mfma_f32_16x16x32_bf16 v[82:85], v[170:173], v[24:27], v[82:85]
	v_mfma_f32_16x16x32_bf16 v[110:113], v[178:181], v[24:27], v[110:113]
	v_mfma_f32_16x16x32_bf16 v[114:117], v[170:173], v[56:59], v[114:117]
	v_mfma_f32_16x16x32_bf16 v[118:121], v[178:181], v[56:59], v[118:121]
	v_mfma_f32_16x16x32_bf16 v[82:85], v[182:185], v[28:31], v[82:85]
	v_mfma_f32_16x16x32_bf16 v[110:113], v[186:189], v[28:31], v[110:113]
	v_mfma_f32_16x16x32_bf16 v[114:117], v[182:185], v[60:63], v[114:117]
	v_mfma_f32_16x16x32_bf16 v[118:121], v[186:189], v[60:63], v[118:121]
	s_setprio 0
	s_nop 3
	v_max_f32_e64 v122, |v83|, |v83|
	v_max_f32_e64 v123, |v82|, |v82|
	v_max_f32_e32 v122, v123, v122
	v_max_f32_e64 v123, |v85|, |v85|
	v_max_f32_e64 v124, |v84|, |v84|
	v_max_f32_e32 v123, v124, v123
	v_max_f32_e64 v124, |v113|, |v113|
	v_max_f32_e64 v125, |v112|, |v112|
	v_max_f32_e32 v124, v125, v124
	v_max3_f32 v124, |v110|, |v111|, v124
	v_max3_f32 v122, v122, v123, v124
	v_mul_f32_e32 v122, 0x3c010204, v122
	v_lshrrev_b32_e32 v123, 23, v122
	v_and_b32_e32 v122, 0x7f800000, v122
	v_sub_u32_e32 v122, 0x7e800000, v122
	v_fmaak_f32 v82, v82, v122, 0x43000000
	v_cvt_pk_u8_f32 v82, v82, 0, 0
	v_fmaak_f32 v83, v83, v122, 0x43000000
	v_cvt_pk_u8_f32 v82, v83, 1, v82
	v_fmaak_f32 v83, v84, v122, 0x43000000
	v_cvt_pk_u8_f32 v82, v83, 2, v82
	v_fmaak_f32 v83, v85, v122, 0x43000000
	v_cvt_pk_u8_f32 v82, v83, 3, v82
	v_fmaak_f32 v83, v110, v122, 0x43000000
	v_cvt_pk_u8_f32 v83, v83, 0, 0
	v_fmaak_f32 v84, v111, v122, 0x43000000
	v_cvt_pk_u8_f32 v83, v84, 1, v83
	v_fmaak_f32 v84, v112, v122, 0x43000000
	v_cvt_pk_u8_f32 v83, v84, 2, v83
	v_fmaak_f32 v84, v113, v122, 0x43000000
	v_cvt_pk_u8_f32 v83, v84, 3, v83
	v_add_u16_e32 v84, 1, v123
	ds_write_b8 v106, v84 offset:140
	v_max_f32_e64 v84, |v115|, |v115|
	v_max_f32_e64 v85, |v114|, |v114|
	v_max_f32_e32 v84, v85, v84
	v_max_f32_e64 v85, |v117|, |v117|
	v_max_f32_e64 v110, |v116|, |v116|
	v_max_f32_e32 v85, v110, v85
	v_max_f32_e64 v110, |v121|, |v121|
	v_max_f32_e64 v111, |v120|, |v120|
	v_max_f32_e32 v110, v111, v110
	v_max3_f32 v110, |v118|, |v119|, v110
	v_max3_f32 v84, v84, v85, v110
	v_mul_f32_e32 v84, 0x3c010204, v84
	v_lshrrev_b32_e32 v110, 23, v84
	v_and_b32_e32 v84, 0x7f800000, v84
	v_sub_u32_e32 v85, 0x7e800000, v84
	v_fmaak_f32 v84, v114, v85, 0x43000000
	v_cvt_pk_u8_f32 v84, v84, 0, 0
	v_fmaak_f32 v111, v115, v85, 0x43000000
	v_cvt_pk_u8_f32 v84, v111, 1, v84
	v_fmaak_f32 v111, v116, v85, 0x43000000
	v_cvt_pk_u8_f32 v84, v111, 2, v84
	v_fmaak_f32 v111, v117, v85, 0x43000000
	v_cvt_pk_u8_f32 v84, v111, 3, v84
	v_fmaak_f32 v111, v118, v85, 0x43000000
	v_cvt_pk_u8_f32 v111, v111, 0, 0
	v_fmaak_f32 v112, v119, v85, 0x43000000
	v_cvt_pk_u8_f32 v111, v112, 1, v111
	v_fmaak_f32 v112, v120, v85, 0x43000000
	v_cvt_pk_u8_f32 v111, v112, 2, v111
	v_fmaak_f32 v85, v121, v85, 0x43000000
	v_cvt_pk_u8_f32 v85, v85, 3, v111
	ds_write2st64_b64 v109, v[82:83], v[84:85] offset1:5
	v_add_u16_e32 v82, 1, v110
	ds_write_b8 v106, v82 offset:2700
	ds_read_b128 v[82:85], v103
	ds_read_b128 v[110:113], v103 offset:1280
	v_lshl_add_u64 v[114:115], s[0:1], 0, v[80:81]
	v_lshl_add_u64 v[118:119], s[0:1], 0, v[78:79]
	s_waitcnt lgkmcnt(0)
	s_cmp_lt_u32 s28, 2
	s_cbranch_scc1 .Ledc_nt5
	global_store_dwordx4 v[114:115], v[82:85], off
	s_branch .Ledc_dn5
.Ledc_nt5:
	global_store_dwordx4 v[114:115], v[82:85], off nt
.Ledc_dn5:
	ds_read_b128 v[82:85], v103 offset:2560
	ds_read_b128 v[114:117], v103 offset:3840
	s_cmp_lt_u32 s28, 2
	s_cbranch_scc1 .Ledc_nt6
	global_store_dwordx4 v[118:119], v[110:113], off
	s_branch .Ledc_dn6
.Ledc_nt6:
	global_store_dwordx4 v[118:119], v[110:113], off nt
.Ledc_dn6:
	s_nop 1
	v_lshl_add_u64 v[110:111], s[0:1], 0, v[76:77]
	s_waitcnt lgkmcnt(0)
	s_cmp_lt_u32 s28, 2
	s_cbranch_scc1 .Ledc_nt7
	global_store_dwordx4 v[110:111], v[82:85], off
	s_branch .Ledc_dn7
.Ledc_nt7:
	global_store_dwordx4 v[110:111], v[82:85], off nt
.Ledc_dn7:
	s_nop 1
	v_lshl_add_u64 v[82:83], s[0:1], 0, v[74:75]
	s_cmp_lt_u32 s28, 2
	s_cbranch_scc1 .Ledc_nt8
	global_store_dwordx4 v[82:83], v[114:117], off
	s_branch .Ledc_dn8
.Ledc_nt8:
	global_store_dwordx4 v[82:83], v[114:117], off nt
.Ledc_dn8:
	s_and_saveexec_b64 s[8:9], s[2:3]
	s_cbranch_execz .LBB0_1287
	ds_read_b128 v[82:85], v104 offset:128
	v_lshl_add_u64 v[110:111], s[0:1], 0, v[72:73]
	s_waitcnt lgkmcnt(0)
	s_cmp_lt_u32 s28, 2
	s_cbranch_scc1 .Ledc_nt9
	global_store_dwordx4 v[110:111], v[82:85], off
	s_branch .Ledc_dn9

; DI void phase_edown3(const Ctx& c, int layer) {
;     ...
;         asm volatile("" ::: "memory");
; DI void grid_sync(const Ctx& c0, XcdBarrier b) { KArgPtr k = c0.kp; asm volatile("" : "+s"(k)); b.bar = (unsigned*)((char*)k[23] + WS_CTL); unsigned x = b.x; asm volatile("" : "+s"(x)); b.x = x; int w = c0.wid; asm volatile("" : "+s"(w));
;     unsigned z = 0u; asm volatile("" : "+v"(z));
;     xcd_barrier(b, w == 0 && __builtin_amdgcn_mbcnt_hi(~0u, __builtin_amdgcn_mbcnt_lo(~0u, z)) == 0u); }
.Ledc_dn9:
	s_branch .LBB0_1287
.LBB0_1292:
	s_mov_b64 s[0:1], s[92:93]
	s_load_dwordx2 s[0:1], s[0:1], 0xb8
	s_mov_b32 s38, s64
	s_mov_b32 s2, s65
	v_mov_b32_e32 v0, v177
	s_cmp_lg_u32 s2, 0
	s_mov_b64 s[2:3], 0
	s_cbranch_scc1 .LBB0_1294
	v_mbcnt_lo_u32_b32 v0, -1, v0
	v_mbcnt_hi_u32_b32 v0, -1, v0
	v_cmp_eq_u32_e32 vcc, 0, v0
	s_and_b64 s[2:3], vcc, exec
